# P2: the SSD unit's dt values and dt_bias/a_log scalars are requested during the retention unit
# speedup vs baseline: 1.0035x; 1.0035x over previous
; #define LAS __attribute__((address_space(3)))
; __device__ __forceinline__ float bf2f(bf16 b) { return __uint_as_float(((unsigned)b) << 16); }
; __device__ __forceinline__ float softplus_f(float x) { return x > 20.f ? x : log1pf(__expf(x)); }
; #define PROJ_AT(X, row, col) (XP_PROJ(X) + (size_t)((col) >> 8) * PANP + (size_t)(row) * 256 + ((col) & 255))
; __device__ __forceinline__ void p2_ret(Ctx& X, int unit) {
;     const int c = unit >> 2, h = unit & 3, t0 = c * CH, tid = X.tid, lane = X.lane, w = X.wave;
;     LAS uchar* Vt = X.lds; LAS uchar* Kt = X.lds + 69632;
;     { u32x4 vv[8], kk[8];
; #pragma unroll
;       for (int i = 0; i < 8; ++i) { const int q = tid + 512 * i, l = q >> 5, vc = q & 31; const bf16* rp = PROJ_AT(X, t0 + l, h * 256 + vc * 8);
;           vv[i] = *(const u32x4*)(rp + (size_t)(C_V >> 8) * PANP); kk[i] = *(const u32x4*)(rp + (size_t)(C_K >> 8) * PANP); }
; #pragma unroll
;       for (int i = 0; i < 8; ++i) { const int q = tid + 512 * i, l = q >> 5, vc = q & 31; *(LAS u32x4*)(Vt + l * 544 + vc * 16) = vv[i]; *(LAS u32x4*)(Kt + l * 544 + vc * 16) = kk[i]; } }
;     __syncthreads();
; __device__ __forceinline__ void p2_ssd(Ctx& X, int unit) {
;     ...
;     if (w < 4) { const int h = 8 * g + 4 * hh + w, l0 = 2 * lane;
;         const float dtb = XP_dt_bias(X)[h], A = -expf(XP_a_log(X)[h]);
;         const float d0 = softplus_f(bf2f(*PROJ_AT(X, t0 + l0, C_DT + h)) + dtb), d1 = softplus_f(bf2f(*PROJ_AT(X, t0 + l0 + 1, C_DT + h)) + dtb);
.LBB0_198:
	s_load_dwordx4 s[12:15], s[0:1], 0x30
	s_lshl_b32 s8, s4, 5
	s_and_b32 s9, s8, 0xffffff80
	s_and_b32 s5, s4, 3
	v_or_b32_e32 v2, s9, v143
	s_lshl_b32 s2, s5, 22
	v_ashrrev_i32_e32 v3, 31, v2
	s_waitcnt vmcnt(1)
	v_lshl_add_u64 v[58:59], v[134:135], 0, s[2:3]
	v_lshlrev_b64 v[2:3], 9, v[2:3]
	v_lshl_add_u64 v[2:3], v[58:59], 0, v[2:3]
	v_add_co_u32_e32 v10, vcc, 0x2000000, v2
	s_lshl_b32 s2, s5, 2
	s_nop 0
	v_addc_co_u32_e32 v11, vcc, 0, v3, vcc
	v_add_co_u32_e32 v12, vcc, 0x1000000, v2
	v_mov_b32_e32 v182, v152
	s_nop 0
	v_addc_co_u32_e32 v13, vcc, 0, v3, vcc
	global_load_dwordx4 v[2:5], v[10:11], off
	global_load_dwordx4 v[6:9], v[12:13], off
	v_or_b32_e32 v10, s9, v145
	v_ashrrev_i32_e32 v11, 31, v10
	v_lshlrev_b64 v[10:11], 9, v[10:11]
	v_lshl_add_u64 v[10:11], v[58:59], 0, v[10:11]
	v_add_co_u32_e32 v18, vcc, s6, v10
	v_mov_b32_e32 v70, 0
	s_nop 0
	v_addc_co_u32_e32 v19, vcc, 0, v11, vcc
	v_add_co_u32_e32 v20, vcc, 0x1000000, v10
	v_mov_b32_e32 v71, v133
	s_nop 0
	v_addc_co_u32_e32 v21, vcc, 0, v11, vcc
	global_load_dwordx4 v[10:13], v[18:19], off
	global_load_dwordx4 v[14:17], v[20:21], off
	v_or_b32_e32 v18, s9, v146
	v_ashrrev_i32_e32 v19, 31, v18
	v_lshlrev_b64 v[18:19], 9, v[18:19]
	v_lshl_add_u64 v[18:19], v[58:59], 0, v[18:19]
	v_add_co_u32_e32 v26, vcc, s6, v18
	v_mov_b32_e32 v72, v133
	s_nop 0
	v_addc_co_u32_e32 v27, vcc, 0, v19, vcc
	v_add_co_u32_e32 v28, vcc, 0x1000000, v18
	v_mov_b32_e32 v73, v133
	s_nop 0
	v_addc_co_u32_e32 v29, vcc, 0, v19, vcc
	global_load_dwordx4 v[18:21], v[26:27], off
	global_load_dwordx4 v[22:25], v[28:29], off
	v_or_b32_e32 v26, s9, v147
	v_ashrrev_i32_e32 v27, 31, v26
	v_lshlrev_b64 v[26:27], 9, v[26:27]
	v_lshl_add_u64 v[26:27], v[58:59], 0, v[26:27]
	v_add_co_u32_e32 v34, vcc, s6, v26
	v_mov_b32_e32 v74, 0
	s_nop 0
	v_addc_co_u32_e32 v35, vcc, 0, v27, vcc
	v_add_co_u32_e32 v36, vcc, 0x1000000, v26
	v_mov_b32_e32 v75, v133
	s_nop 0
	v_addc_co_u32_e32 v37, vcc, 0, v27, vcc
	global_load_dwordx4 v[26:29], v[34:35], off
	global_load_dwordx4 v[30:33], v[36:37], off
	v_or_b32_e32 v34, s9, v148
	v_ashrrev_i32_e32 v35, 31, v34
	v_lshlrev_b64 v[34:35], 9, v[34:35]
	v_lshl_add_u64 v[34:35], v[58:59], 0, v[34:35]
	v_add_co_u32_e32 v42, vcc, s6, v34
	s_waitcnt vmcnt(8)
	v_mov_b32_e32 v76, v133
	v_addc_co_u32_e32 v43, vcc, 0, v35, vcc
	v_add_co_u32_e32 v44, vcc, 0x1000000, v34
	v_mov_b32_e32 v77, v133
	s_nop 0
	v_addc_co_u32_e32 v45, vcc, 0, v35, vcc
	global_load_dwordx4 v[34:37], v[42:43], off
	global_load_dwordx4 v[38:41], v[44:45], off
	v_or_b32_e32 v42, s9, v149
	v_ashrrev_i32_e32 v43, 31, v42
	v_lshlrev_b64 v[42:43], 9, v[42:43]
	v_lshl_add_u64 v[42:43], v[58:59], 0, v[42:43]
	v_add_co_u32_e32 v50, vcc, s6, v42
	v_mov_b32_e32 v78, 0
	s_nop 0
	v_addc_co_u32_e32 v51, vcc, 0, v43, vcc
	v_add_co_u32_e32 v52, vcc, 0x1000000, v42
	v_mov_b32_e32 v79, v133
	s_nop 0
	v_addc_co_u32_e32 v53, vcc, 0, v43, vcc
	global_load_dwordx4 v[42:45], v[50:51], off
	global_load_dwordx4 v[46:49], v[52:53], off
	v_or_b32_e32 v50, s8, v150
	v_ashrrev_i32_e32 v51, 31, v50
	v_lshlrev_b64 v[50:51], 9, v[50:51]
	v_lshl_add_u64 v[50:51], v[58:59], 0, v[50:51]
	v_add_co_u32_e32 v60, vcc, s6, v50
	v_mov_b32_e32 v80, v133
	s_nop 0
	v_addc_co_u32_e32 v61, vcc, 0, v51, vcc
	v_add_co_u32_e32 v62, vcc, 0x1000000, v50
	v_mov_b32_e32 v81, v133
	s_nop 0
	v_addc_co_u32_e32 v63, vcc, 0, v51, vcc
	global_load_dwordx4 v[50:53], v[60:61], off
	global_load_dwordx4 v[54:57], v[62:63], off
	v_or_b32_e32 v60, s9, v151
	v_ashrrev_i32_e32 v61, 31, v60
	v_lshlrev_b64 v[60:61], 9, v[60:61]
	v_lshl_add_u64 v[58:59], v[58:59], 0, v[60:61]
	v_add_co_u32_e32 v66, vcc, s6, v58
	s_getpc_b64 s[8:9]
	s_add_u32 s8, s8, LG2_GAMMA@rel32@lo+4
	s_addc_u32 s9, s9, LG2_GAMMA@rel32@hi+12
	s_nop 0
	s_load_dword s2, s[8:9], s2 offset:0x0
	v_addc_co_u32_e32 v67, vcc, 0, v59, vcc
	v_add_co_u32_e32 v68, vcc, 0x1000000, v58
	v_mov_b32_e32 v82, 0
	s_nop 0
	v_addc_co_u32_e32 v69, vcc, 0, v59, vcc
	global_load_dwordx4 v[58:61], v[66:67], off
	global_load_dwordx4 v[62:65], v[68:69], off
	v_mov_b32_e32 v66, 0
	v_mov_b32_e32 v67, v133
	v_mov_b32_e32 v68, v133
	v_mov_b32_e32 v69, v133
	v_mov_b32_e32 v83, v133
	v_mov_b32_e32 v84, v133
	v_mov_b32_e32 v85, v133
	v_mov_b32_e32 v86, 0
	v_mov_b32_e32 v87, v133
	v_mov_b32_e32 v88, v133
	v_mov_b32_e32 v89, v133
	v_mov_b32_e32 v90, 0
	v_mov_b32_e32 v91, v133
	s_waitcnt vmcnt(15)
	ds_write_b128 v155, v[2:5]
	s_waitcnt vmcnt(14)
	ds_write_b128 v156, v[6:9]
	s_waitcnt vmcnt(13)
	ds_write_b128 v157, v[10:13]
	s_waitcnt vmcnt(12)
	ds_write_b128 v159, v[14:17]
	s_waitcnt vmcnt(11)
	ds_write_b128 v155, v[18:21] offset:17408
	s_waitcnt vmcnt(10)
	ds_write_b128 v156, v[22:25] offset:17408
	s_waitcnt vmcnt(9)
	ds_write_b128 v160, v[26:29]
	s_waitcnt vmcnt(8)
	ds_write_b128 v161, v[30:33]
	s_waitcnt vmcnt(7)
	ds_write_b128 v155, v[34:37] offset:34816
	s_waitcnt vmcnt(6)
	ds_write_b128 v156, v[38:41] offset:34816
	s_waitcnt vmcnt(5)
	ds_write_b128 v162, v[42:45]
	s_waitcnt vmcnt(4)
	ds_write_b128 v163, v[46:49]
	s_waitcnt vmcnt(3)
	ds_write_b128 v155, v[50:53] offset:52224
	s_waitcnt vmcnt(2)
	ds_write_b128 v156, v[54:57] offset:52224
	s_waitcnt vmcnt(1)
	ds_write_b128 v164, v[58:61]
	s_waitcnt vmcnt(0)
	ds_write_b128 v165, v[62:65]
	s_waitcnt lgkmcnt(0)
	s_barrier
	s_cmpk_lg_i32 s92, 0x100
	s_cbranch_scc1 .Lp2pre_skip
	s_cmp_ge_u32 s93, 4
	s_cbranch_scc1 .Lp2pre_skip
	s_and_b32 s10, s4, 3
	s_lshl_b32 s10, s10, 2
	s_add_i32 s10, s10, s93
	s_lshl_b32 s11, s4, 5
	s_and_b32 s11, s11, 0xffffff80
	v_lshlrev_b32_e32 v254, 1, v194
	v_or_b32_e32 v254, s11, v254
	v_lshlrev_b32_e32 v254, 9, v254
	s_lshl_b32 s11, s10, 1
	v_add_u32_e32 v254, s11, v254
	s_add_u32 s16, s90, 0x1a800000
	s_addc_u32 s17, s91, 0
	global_load_ushort v252, v254, s[16:17] offset:512
	global_load_ushort v253, v254, s[16:17]
	s_lshl_b32 s11, s10, 2
	v_mov_b32_e32 v255, s11
	global_load_dword v254, v255, s[12:13]
	global_load_dword v255, v255, s[14:15]
; __device__ __forceinline__ void p2_ret(Ctx& X, int unit) {
;     ...
;     const float lg = LG2_GAMMA[h];
;     float rr[8];
; #pragma unroll
;     for (int e = 0; e < 8; ++e) rr[e] = exp2f(-lg * (float)e);
;     const int fr = lane & 15, fq = lane >> 4, trs = (8 * fq + ((lane & 15) >> 2)) * 544 + 8 * (lane & 3);
;     f32x4 acc[2][16];
; #pragma unroll
;     for (int a = 0; a < 2; ++a)
; #pragma unroll
;         for (int n = 0; n < 16; ++n) acc[a][n] = (f32x4){0.f, 0.f, 0.f, 0.f};
.Lp2pre_skip:
	v_mov_b32_e32 v4, v133
	v_mov_b32_e32 v5, v133
	v_mov_b32_e32 v6, 0
	v_mov_b32_e32 v7, v133
	s_waitcnt lgkmcnt(0)
	v_mul_f32_e32 v2, s2, v166
	v_cmp_gt_f32_e32 vcc, s7, v2
	s_and_b64 s[8:9], vcc, exec
	s_cselect_b32 s5, 0xffffffc0, 0
	v_cndmask_b32_e32 v2, 0, v167, vcc
	v_cmp_gt_f32_e32 vcc, s2, v168
	v_fmac_f32_e32 v2, s2, v166
	v_exp_f32_e32 v2, v2
	v_cndmask_b32_e32 v3, 0, v167, vcc
	v_subrev_f32_e32 v3, s2, v3
	v_exp_f32_e32 v3, v3
	s_and_b64 s[8:9], vcc, exec
	v_ldexp_f32 v174, v2, s5
	s_cselect_b32 s5, 0xffffffc0, 0
	v_mul_f32_e64 v2, s2, -2.0
	v_ldexp_f32 v175, v3, s5
	v_cmp_gt_f32_e32 vcc, s7, v2
	v_mul_f32_e32 v3, s2, v169
	s_and_b64 s[8:9], vcc, exec
	v_cndmask_b32_e32 v2, 0, v167, vcc
	v_cmp_gt_f32_e32 vcc, s7, v3
	v_fmac_f32_e64 v2, s2, -2.0
	v_exp_f32_e32 v2, v2
	v_cndmask_b32_e32 v3, 0, v167, vcc
	v_fmac_f32_e32 v3, s2, v169
	v_exp_f32_e32 v3, v3
	s_cselect_b32 s5, 0xffffffc0, 0
	s_and_b64 s[8:9], vcc, exec
	v_ldexp_f32 v176, v2, s5
	s_cselect_b32 s5, 0xffffffc0, 0
	v_mul_f32_e64 v2, s2, -4.0
	v_ldexp_f32 v177, v3, s5
	v_cmp_gt_f32_e32 vcc, s7, v2
	v_mul_f32_e32 v3, s2, v170
	s_and_b64 s[8:9], vcc, exec
	v_cndmask_b32_e32 v2, 0, v167, vcc
	v_cmp_gt_f32_e32 vcc, s7, v3
	v_fmac_f32_e64 v2, s2, -4.0
	v_exp_f32_e32 v2, v2
	v_cndmask_b32_e32 v3, 0, v167, vcc
	v_fmac_f32_e32 v3, s2, v170
	v_exp_f32_e32 v3, v3
	s_cselect_b32 s5, 0xffffffc0, 0
	s_and_b64 s[8:9], vcc, exec
	v_ldexp_f32 v178, v2, s5
	s_cselect_b32 s5, 0xffffffc0, 0
	v_mul_f32_e32 v2, s2, v171
	v_ldexp_f32 v179, v3, s5
	v_cmp_gt_f32_e32 vcc, s7, v2
	v_mul_f32_e32 v3, s2, v172
	s_and_b64 s[8:9], vcc, exec
	v_cndmask_b32_e32 v2, 0, v167, vcc
	v_cmp_gt_f32_e32 vcc, s7, v3
	v_fmac_f32_e32 v2, s2, v171
	v_exp_f32_e32 v2, v2
	v_cndmask_b32_e32 v3, 0, v167, vcc
	v_fmac_f32_e32 v3, s2, v172
	v_exp_f32_e32 v3, v3
	s_cselect_b32 s5, 0xffffffc0, 0
	s_and_b64 s[8:9], vcc, exec
	v_ldexp_f32 v180, v2, s5
	s_cselect_b32 s5, 0xffffffc0, 0
	v_ldexp_f32 v181, v3, s5
	s_mov_b32 s5, 0
	v_mov_b32_e32 v2, 0
	v_mov_b32_e32 v3, v133
	v_mov_b32_e32 v8, v133
	v_mov_b32_e32 v9, v133
	v_mov_b32_e32 v10, 0
	v_mov_b32_e32 v11, v133
	v_mov_b32_e32 v12, v133
	v_mov_b32_e32 v13, v133
	v_mov_b32_e32 v14, 0
	v_mov_b32_e32 v15, v133
	v_mov_b32_e32 v16, v133
	v_mov_b32_e32 v17, v133
	v_mov_b32_e32 v18, 0
	v_mov_b32_e32 v19, v133
	v_mov_b32_e32 v20, v133
	v_mov_b32_e32 v21, v133
	v_mov_b32_e32 v22, 0
	v_mov_b32_e32 v23, v133
	v_mov_b32_e32 v24, v133
	v_mov_b32_e32 v25, v133
	v_mov_b32_e32 v26, 0
	v_mov_b32_e32 v27, v133
	v_mov_b32_e32 v28, v133
	v_mov_b32_e32 v29, v133
	v_mov_b32_e32 v30, 0
	v_mov_b32_e32 v31, v133
	v_mov_b32_e32 v32, v133
	v_mov_b32_e32 v33, v133
	v_mov_b32_e32 v34, 0
	v_mov_b32_e32 v35, v133
	v_mov_b32_e32 v36, v133
	v_mov_b32_e32 v37, v133
	v_mov_b32_e32 v38, 0
	v_mov_b32_e32 v39, v133
	v_mov_b32_e32 v40, v133
	v_mov_b32_e32 v41, v133
	v_mov_b32_e32 v42, 0
	v_mov_b32_e32 v43, v133
	v_mov_b32_e32 v44, v133
	v_mov_b32_e32 v45, v133
	v_mov_b32_e32 v46, 0
	v_mov_b32_e32 v47, v133
	v_mov_b32_e32 v48, v133
	v_mov_b32_e32 v49, v133
	v_mov_b32_e32 v50, 0
	v_mov_b32_e32 v51, v133
	v_mov_b32_e32 v52, v133
	v_mov_b32_e32 v53, v133
	v_mov_b32_e32 v54, 0
	v_mov_b32_e32 v55, v133
	v_mov_b32_e32 v56, v133
	v_mov_b32_e32 v57, v133
	v_mov_b32_e32 v58, 0
	v_mov_b32_e32 v59, v133
	v_mov_b32_e32 v60, v133
	v_mov_b32_e32 v61, v133
	v_mov_b32_e32 v62, 0
	v_mov_b32_e32 v63, v133
	v_mov_b32_e32 v64, v133
	v_mov_b32_e32 v65, v133
	v_mov_b32_e32 v92, v133
	v_mov_b32_e32 v93, v133
	v_mov_b32_e32 v94, 0
	v_mov_b32_e32 v95, v133
	v_mov_b32_e32 v96, v133
	v_mov_b32_e32 v97, v133
	v_mov_b32_e32 v98, 0
	v_mov_b32_e32 v99, v133
	v_mov_b32_e32 v100, v133
	v_mov_b32_e32 v101, v133
	v_mov_b32_e32 v102, 0
	v_mov_b32_e32 v103, v133
	v_mov_b32_e32 v104, v133
	v_mov_b32_e32 v105, v133
	v_mov_b32_e32 v106, 0
	v_mov_b32_e32 v107, v133
	v_mov_b32_e32 v108, v133
	v_mov_b32_e32 v109, v133
	v_mov_b32_e32 v110, 0
	v_mov_b32_e32 v111, v133
	v_mov_b32_e32 v112, v133
	v_mov_b32_e32 v113, v133
	v_mov_b32_e32 v114, 0
	v_mov_b32_e32 v115, v133
	v_mov_b32_e32 v116, v133
	v_mov_b32_e32 v117, v133
	v_mov_b32_e32 v118, 0
	v_mov_b32_e32 v119, v133
	v_mov_b32_e32 v120, v133
	v_mov_b32_e32 v121, v133
	v_mov_b32_e32 v122, 0
	v_mov_b32_e32 v123, v133
	v_mov_b32_e32 v124, v133
	v_mov_b32_e32 v125, v133
	v_mov_b32_e32 v126, 0
	v_mov_b32_e32 v127, v133
	v_mov_b32_e32 v128, v133
	v_mov_b32_e32 v129, v133

; __device__ __forceinline__ float bf2f(bf16 b) { return __uint_as_float(((unsigned)b) << 16); }
; __device__ __forceinline__ float softplus_f(float x) { return x > 20.f ? x : log1pf(__expf(x)); }
; #define PROJ_AT(X, row, col) (XP_PROJ(X) + (size_t)((col) >> 8) * PANP + (size_t)(row) * 256 + ((col) & 255))
; __device__ __forceinline__ void p2_ssd(Ctx& X, int unit) {
;     ...
;     if (w < 4) { const int h = 8 * g + 4 * hh + w, l0 = 2 * lane;
;         const float dtb = XP_dt_bias(X)[h], A = -expf(XP_a_log(X)[h]);
;         const float d0 = softplus_f(bf2f(*PROJ_AT(X, t0 + l0, C_DT + h)) + dtb), d1 = softplus_f(bf2f(*PROJ_AT(X, t0 + l0 + 1, C_DT + h)) + dtb);
;         const float a0 = d0 * A, a1 = d1 * A, s = a0 + a1, incl = wave_incl_scan(s, lane);
;         dtS[w * 128 + l0] = d0; dtS[w * 128 + l0 + 1] = d1; acS[w * 128 + l0] = incl - a1; acS[w * 128 + l0 + 1] = incl;
;         if (lane == 63) XP_ADEC(X)[c * 16 + h] = expf(incl); }
.LBB0_202:
	s_load_dwordx2 s[98:99], s[0:1], 0x20
	s_load_dwordx2 s[100:101], s[0:1], 0x28
	s_ashr_i32 s71, s70, 2
	s_bfe_u32 s72, s70, 0x10001
	s_and_b32 s73, s70, 1
	s_andn2_b64 vcc, exec, s[30:31]
	s_lshl_b32 s74, s71, 7
	s_cbranch_vccnz .LBB0_210
	s_lshl_b32 s36, s72, 3
	s_lshl_b32 s48, s73, 2
	s_or_b32 s36, s36, s48
	v_or_b32_e32 v4, s74, v145
	s_or_b32 s50, s36, s93
	s_load_dwordx4 s[52:55], s[0:1], 0x30
	v_ashrrev_i32_e32 v5, 31, v4
	s_lshl_b32 s36, s50, 2
	v_lshlrev_b64 v[2:3], 9, v[4:5]
	v_mov_b32_e32 v6, s36
	v_lshl_add_u64 v[2:3], s[34:35], 0, v[2:3]
	s_lshl_b32 s36, s50, 1
	v_lshl_add_u64 v[2:3], v[2:3], 0, s[36:37]
	s_cmpk_eq_i32 s92, 0x100
	s_cbranch_scc1 .Lp2pre_have
	global_load_ushort v252, v[2:3], off offset:512
	global_load_ushort v2, v[2:3], off
	s_waitcnt lgkmcnt(0)
	global_load_dword v3, v6, s[52:53]
	global_load_dword v5, v6, s[54:55]
	s_branch .Lp2pre_join
.Lp2pre_have:
	s_waitcnt vmcnt(0) lgkmcnt(0)
	v_mov_b32_e32 v2, v253
	v_mov_b32_e32 v3, v254
	v_mov_b32_e32 v5, v255
.Lp2pre_join:
	s_waitcnt vmcnt(2)
	v_lshlrev_b32_e32 v2, 16, v2
	s_waitcnt vmcnt(1)
	v_add_f32_e32 v2, v3, v2
	v_cmp_nlt_f32_e32 vcc, s61, v2
	s_and_saveexec_b64 s[48:49], vcc
	s_cbranch_execz .LBB0_205
	v_mul_f32_e32 v2, 0x3fb8aa3b, v2
	v_exp_f32_e32 v2, v2
	s_nop 0
	v_add_f32_e32 v8, 1.0, v2
	v_frexp_mant_f32_e32 v10, v8
	v_cvt_f64_f32_e32 v[6:7], v8
	v_frexp_exp_i32_f64_e32 v6, v[6:7]
	v_cmp_gt_f32_e32 vcc, s63, v10
	v_add_f32_e32 v9, -1.0, v8
	v_sub_f32_e32 v11, v9, v8
	v_subbrev_co_u32_e32 v14, vcc, 0, v6, vcc
	v_sub_u32_e32 v6, 0, v14
	v_sub_f32_e32 v9, v2, v9
	v_add_f32_e32 v11, 1.0, v11
	v_ldexp_f32 v7, v8, v6
	v_add_f32_e32 v9, v9, v11
	v_add_f32_e32 v8, -1.0, v7
	v_add_f32_e32 v10, 1.0, v7
	v_ldexp_f32 v6, v9, v6
	v_add_f32_e32 v9, 1.0, v8
	v_add_f32_e32 v11, -1.0, v10
	v_sub_f32_e32 v9, v7, v9
	v_sub_f32_e32 v7, v7, v11
	v_add_f32_e32 v9, v6, v9
	v_add_f32_e32 v6, v6, v7
	v_add_f32_e32 v15, v10, v6
	v_rcp_f32_e32 v17, v15
	v_sub_f32_e32 v7, v15, v10
	v_sub_f32_e32 v16, v6, v7
	v_add_f32_e32 v7, v8, v9
	v_mul_f32_e32 v19, v7, v17
	v_sub_f32_e32 v6, v7, v8
	v_mul_f32_e32 v8, v15, v19
	v_fma_f32 v10, v19, v15, -v8
	v_fmac_f32_e32 v10, v19, v16
	v_sub_f32_e32 v18, v9, v6
	v_add_f32_e32 v6, v8, v10
	v_sub_f32_e32 v9, v7, v6
	v_pk_add_f32 v[12:13], v[6:7], v[8:9] neg_lo:[0,1] neg_hi:[0,1]
	v_mov_b32_e32 v11, v6
	v_pk_add_f32 v[6:7], v[12:13], v[10:11] neg_lo:[0,1] neg_hi:[0,1]
	v_cmp_neq_f32_e32 vcc, s65, v2
	v_add_f32_e32 v7, v18, v7
	v_add_f32_e32 v6, v6, v7
	v_add_f32_e32 v7, v9, v6
	v_mul_f32_e32 v18, v17, v7
	v_mul_f32_e32 v8, v15, v18
	v_fma_f32 v10, v18, v15, -v8
	v_fmac_f32_e32 v10, v18, v16
	v_sub_f32_e32 v9, v9, v7
	v_add_f32_e32 v15, v6, v9
	v_add_f32_e32 v6, v8, v10
	v_sub_f32_e32 v9, v7, v6
	v_pk_add_f32 v[12:13], v[6:7], v[8:9] neg_lo:[0,1] neg_hi:[0,1]
	v_mov_b32_e32 v11, v6
	v_pk_add_f32 v[6:7], v[12:13], v[10:11] neg_lo:[0,1] neg_hi:[0,1]
	s_nop 0
	v_add_f32_e32 v7, v15, v7
	v_add_f32_e32 v6, v6, v7
	v_add_f32_e32 v7, v19, v18
	v_add_f32_e32 v6, v9, v6
	v_sub_f32_e32 v8, v7, v19
	v_mul_f32_e32 v6, v17, v6
	v_sub_f32_e32 v8, v18, v8
	v_add_f32_e32 v8, v8, v6
	v_add_f32_e32 v10, v7, v8
	v_mul_f32_e32 v11, v10, v10
	v_fmamk_f32 v6, v11, 0x3e9b6dac, v221
	v_fmaak_f32 v103, v11, v6, 0x3f2aaada
	v_cvt_f32_i32_e32 v6, v14
	v_sub_f32_e32 v7, v10, v7
	v_sub_f32_e32 v7, v8, v7
	v_ldexp_f32 v12, v7, 1
	v_mul_f32_e32 v7, v10, v11
	v_ldexp_f32 v9, v10, 1
	v_pk_mul_f32 v[10:11], v[6:7], v[102:103]
	s_nop 0
	v_fma_f32 v8, v6, s64, -v10
	v_fmac_f32_e32 v8, 0xb102e308, v6
	v_pk_add_f32 v[6:7], v[10:11], v[8:9]
	s_nop 0
	v_sub_f32_e32 v9, v7, v9
	v_sub_f32_e32 v9, v11, v9
	v_add_f32_e32 v13, v12, v9
	v_mov_b32_e32 v12, v10
	v_pk_add_f32 v[10:11], v[6:7], v[10:11] neg_lo:[0,1] neg_hi:[0,1]
	v_pk_add_f32 v[14:15], v[6:7], v[12:13]
	v_mov_b32_e32 v9, v6
	v_mov_b32_e32 v11, v15
	v_pk_add_f32 v[16:17], v[8:9], v[10:11] neg_lo:[0,1] neg_hi:[0,1]
	v_pk_add_f32 v[8:9], v[8:9], v[10:11]
	v_mov_b32_e32 v12, v13
	v_pk_add_f32 v[10:11], v[8:9], v[6:7] op_sel:[1,0] op_sel_hi:[0,1] neg_lo:[0,1] neg_hi:[0,1]
	v_pk_add_f32 v[18:19], v[14:15], v[10:11] op_sel_hi:[1,0] neg_lo:[0,1] neg_hi:[0,1]
	v_mov_b32_e32 v14, v15
	v_mov_b32_e32 v15, v9
	v_pk_mov_b32 v[10:11], v[6:7], v[10:11] op_sel:[1,0]
	v_mov_b32_e32 v13, v6
	v_pk_add_f32 v[10:11], v[14:15], v[10:11] neg_lo:[0,1] neg_hi:[0,1]
	v_mov_b32_e32 v18, v16
	v_pk_add_f32 v[6:7], v[12:13], v[10:11] neg_lo:[0,1] neg_hi:[0,1]
	v_mov_b32_e32 v17, v9
	v_pk_add_f32 v[10:11], v[18:19], v[6:7]
	s_nop 0
	v_pk_add_f32 v[12:13], v[10:11], v[10:11] op_sel:[0,1] op_sel_hi:[1,0]
	s_nop 0
	v_pk_add_f32 v[8:9], v[8:9], v[12:13] op_sel:[1,0] op_sel_hi:[0,1]
	v_mov_b32_e32 v11, v8
	v_pk_add_f32 v[14:15], v[10:11], v[16:17] neg_lo:[0,1] neg_hi:[0,1]
	v_mov_b32_e32 v7, v12
	v_sub_f32_e32 v9, v10, v14
	v_pk_add_f32 v[6:7], v[6:7], v[14:15] neg_lo:[0,1] neg_hi:[0,1]
	v_sub_f32_e32 v9, v16, v9
	v_add_f32_e32 v6, v6, v9
	v_add_f32_e32 v6, v6, v7
	v_add_f32_e32 v6, v8, v6
	v_cndmask_b32_e32 v6, v223, v6, vcc
	v_cmp_ngt_f32_e32 vcc, -1.0, v2
	s_nop 1
	v_cndmask_b32_e32 v6, v224, v6, vcc
	v_cmp_neq_f32_e32 vcc, -1.0, v2
	s_nop 1
	v_cndmask_b32_e32 v6, v225, v6, vcc
	v_cmp_lt_f32_e64 vcc, |v2|, s66
	s_nop 1
	v_cndmask_b32_e32 v2, v6, v2, vcc
